# MLA finalize: row loads requested one row ahead (software prefetch into spare VGPRs)
# speedup vs baseline: 1.0239x; 1.0057x over previous
.LBB0_594:
	s_or_b64 exec, exec, s[0:1]
	s_mov_b32 s72, s73
	v_readlane_b32 s12, v254, 4
	v_readlane_b32 s13, v254, 2
	v_readlane_b32 s0, v254, 3
	s_waitcnt lgkmcnt(0)
	s_barrier
	s_mov_b32 s6, 15
	s_mov_b32 s0, 16
	v_mov_b32_e32 v2, v0
	s_lshl_b32 s2, s12, 3
	v_readfirstlane_b32 s1, v2
	s_ashr_i32 s1, s1, 6
	s_add_i32 s4, s1, s2
	s_cmpk_lt_i32 s4, 0x4000
	s_cbranch_scc0 .LBB0_597
	s_ashr_i32 s7, s6, 31
	s_lshl_b64 s[2:3], s[6:7], 3
	s_add_u32 s2, s94, s2
	s_addc_u32 s3, s95, s3
	s_load_dwordx2 s[2:3], s[2:3], 0x0
	s_mul_i32 s6, s76, 0xc0
	s_mov_b32 s7, s73
	s_lshl_b64 s[6:7], s[6:7], 2
	v_and_b32_e32 v1, 7, v2
	s_waitcnt lgkmcnt(0)
	s_add_u32 s2, s2, s6
	s_addc_u32 s3, s3, s7
	s_ashr_i32 s1, s0, 31
	s_lshl_b64 s[0:1], s[0:1], 3
	s_add_u32 s0, s94, s0
	s_addc_u32 s1, s95, s1
	s_load_dwordx2 s[0:1], s[0:1], 0x0
	v_lshlrev_b32_e32 v16, 6, v1
	v_lshlrev_b32_e32 v72, 4, v1
	v_lshlrev_b32_e32 v58, 2, v1
	v_bfe_u32 v17, v2, 3, 3
	s_waitcnt lgkmcnt(0)
	s_add_u32 s0, s0, s6
	s_addc_u32 s1, s1, s7
	global_load_dwordx4 v[4:7], v16, s[2:3]
	global_load_dwordx4 v[8:11], v16, s[2:3] offset:16
	global_load_dwordx4 v[12:15], v16, s[2:3] offset:32
	global_load_dwordx4 v[20:23], v16, s[2:3] offset:48
	global_load_dwordx4 v[24:27], v16, s[0:1]
	global_load_dwordx4 v[28:31], v16, s[0:1] offset:16
	global_load_dwordx4 v[32:35], v16, s[0:1] offset:32
	global_load_dwordx4 v[36:39], v16, s[0:1] offset:48
	global_load_dwordx4 v[40:43], v72, s[2:3] offset:512
	global_load_dwordx4 v[44:47], v72, s[2:3] offset:640
	global_load_dwordx4 v[48:51], v72, s[0:1] offset:512
	global_load_dwordx4 v[52:55], v72, s[0:1] offset:640
	v_or_b32_e32 v16, 3, v58
	v_cvt_f32_ubyte0_e32 v16, v16
	v_mul_f32_e32 v16, 0xbed49a78, v16
	v_exp_f32_e32 v56, v16
	v_or_b32_e32 v16, 2, v58
	v_cvt_f32_ubyte0_e32 v16, v16
	v_mul_f32_e32 v16, 0xbed49a78, v16
	v_exp_f32_e32 v57, v16
	v_and_b32_e32 v19, 64, v222
	s_ashr_i32 s5, s4, 31
	v_readlane_b32 s16, v254, 15
	s_lshl_b32 s6, s13, 3
	v_or_b32_e32 v16, 1, v58
	v_mul_u32_u24_e32 v2, 0xc0, v17
	v_lshlrev_b32_e32 v68, 8, v17
	v_xor_b32_e32 v17, 1, v222
	v_add_u32_e32 v60, 64, v19
	s_lshl_b64 s[0:1], s[4:5], 11
	v_readlane_b32 s18, v254, 17
	v_cvt_f32_ubyte0_e32 v16, v16
	v_cmp_lt_i32_e32 vcc, v17, v60
	v_readlane_b32 s19, v254, 18
	s_add_u32 s2, s18, s0
	v_mul_f32_e32 v16, 0xbed49a78, v16
	v_cndmask_b32_e32 v17, v222, v17, vcc
	v_cvt_f64_f32_e32 v[62:63], v57
	v_cvt_f64_f32_e32 v[64:65], v56
	v_lshlrev_b32_e32 v56, 3, v1
	v_mov_b32_e32 v57, v3
	s_addc_u32 s3, s19, s1
	v_exp_f32_e32 v59, v16
	v_cvt_f32_ubyte0_e32 v16, v58
	v_lshlrev_b32_e32 v19, 2, v17
	v_xor_b32_e32 v17, 2, v222
	v_lshl_add_u64 v[66:67], s[2:3], 0, v[56:57]
	v_or3_b32 v56, s0, v68, v72
	v_mov_b32_e32 v57, s1
	v_readlane_b32 s0, v254, 8
	v_mul_f32_e32 v16, 0xbed49a78, v16
	v_cmp_lt_i32_e32 vcc, v17, v60
	v_readlane_b32 s1, v254, 9
	v_exp_f32_e32 v16, v16
	v_cndmask_b32_e32 v17, v222, v17, vcc
	v_lshl_add_u64 v[68:69], s[0:1], 0, v[56:57]
	s_mul_hi_i32 s0, s4, 0x600
	s_mul_i32 s1, s4, 0x600
	v_lshlrev_b32_e32 v94, 2, v17
	v_xor_b32_e32 v17, 4, v222
	v_or_b32_e32 v56, s1, v58
	v_mov_b32_e32 v57, s0
	v_cmp_lt_i32_e32 vcc, v17, v60
	v_cvt_f64_f32_e32 v[60:61], v59
	v_lshl_add_u64 v[58:59], v[56:57], 0, v[2:3]
	v_or_b32_e32 v56, s1, v72
	v_cndmask_b32_e32 v17, v222, v17, vcc
	s_ashr_i32 s7, s6, 31
	v_lshl_add_u64 v[56:57], v[56:57], 0, v[2:3]
	s_mov_b32 s2, 0x6dc9c883
	v_lshlrev_b32_e32 v95, 2, v17
	v_cvt_f64_f32_e32 v[16:17], v16
	s_lshl_b64 s[8:9], s[6:7], 11
	v_lshl_add_u64 v[70:71], s[18:19], 0, v[58:59]
	s_mul_i32 s10, s13, 0x3000
	s_mul_hi_i32 s11, s6, 0x600
	v_lshl_add_u64 v[72:73], s[18:19], 0, v[56:57]
	s_mov_b32 s3, 0x3fc45f30
	s_mov_b32 s5, 0xb000000
	s_mov_b32 s7, 0x3f553b94
	s_mov_b32 s14, 0x12000000
	v_readlane_b32 s17, v254, 16
	s_mov_b32 s100, 0xb000000
	s_mov_b32 s101, 0
	v_lshl_add_u64 v[142:143], v[72:73], 0, s[72:73]
	v_lshl_add_u64 v[144:145], v[70:71], 0, s[72:73]
	v_lshl_add_u64 v[146:147], v[68:69], 0, s[72:73]
	v_lshl_add_u64 v[148:149], v[66:67], 0, s[72:73]
	v_lshl_add_u64 v[142:143], v[142:143], 0, s[100:101]
	v_lshl_add_u64 v[144:145], v[144:145], 0, s[100:101]
	s_mov_b32 s100, 0x4000000
	v_lshl_add_u64 v[148:149], v[148:149], 0, s[100:101]
	global_load_dwordx4 v[128:131], v[142:143], off
	global_load_dword v132, v[144:145], off offset:128
	global_load_dword v133, v[144:145], off offset:160
	global_load_dwordx4 v[134:137], v[146:147], off
	global_load_dwordx2 v[138:139], v[148:149], off offset:1536
	global_load_dwordx2 v[140:141], v[148:149], off offset:1600
	s_waitcnt vmcnt(0)
.LBB0_596:
	s_and_b32 s0, s4, 0x1fff
	v_cvt_f64_u32_e32 v[56:57], s0
	v_mul_f64 v[58:59], v[16:17], v[56:57]
	v_mul_f64 v[74:75], v[58:59], s[2:3]
	v_rndne_f64_e32 v[74:75], v[74:75]
	v_fma_f64 v[58:59], v[58:59], s[2:3], -v[74:75]
	v_cvt_f32_f64_e32 v1, v[58:59]
	v_mul_f64 v[58:59], v[60:61], v[56:57]
	v_mul_f64 v[74:75], v[58:59], s[2:3]
	v_rndne_f64_e32 v[74:75], v[74:75]
	v_fma_f64 v[58:59], v[58:59], s[2:3], -v[74:75]
	v_sin_f32_e32 v99, v1
	v_cos_f32_e32 v102, v1
	v_cvt_f32_f64_e32 v1, v[58:59]
	v_mul_f64 v[58:59], v[62:63], v[56:57]
	v_mul_f64 v[74:75], v[58:59], s[2:3]
	v_rndne_f64_e32 v[74:75], v[74:75]
	v_fma_f64 v[58:59], v[58:59], s[2:3], -v[74:75]
	v_mul_f64 v[56:57], v[64:65], v[56:57]
	v_sin_f32_e32 v97, v1
	v_cos_f32_e32 v101, v1
	v_cvt_f32_f64_e32 v1, v[58:59]
	v_mul_f64 v[58:59], v[56:57], s[2:3]
	v_rndne_f64_e32 v[58:59], v[58:59]
	v_fma_f64 v[56:57], v[56:57], s[2:3], -v[58:59]
	v_lshl_add_u64 v[76:77], v[72:73], 0, s[72:73]
	v_sin_f32_e32 v96, v1
	v_cos_f32_e32 v100, v1
	v_cvt_f32_f64_e32 v1, v[56:57]
	v_add_co_u32_e32 v56, vcc, s5, v76
	v_lshl_add_u64 v[74:75], v[70:71], 0, s[72:73]
	s_nop 0
	v_addc_co_u32_e32 v57, vcc, 0, v77, vcc
	v_lshl_add_u64 v[142:143], v[56:57], 0, s[10:11]
	v_add_co_u32_e32 v56, vcc, s5, v74
	v_sin_f32_e32 v2, v1
	s_nop 0
	v_addc_co_u32_e32 v57, vcc, 0, v75, vcc
	v_cos_f32_e32 v98, v1
	v_lshl_add_u64 v[144:145], v[56:57], 0, s[10:11]
	v_lshl_add_u64 v[56:57], v[68:69], 0, s[72:73]
	v_lshl_add_u64 v[146:147], v[56:57], 0, s[8:9]
	v_lshl_add_u64 v[78:79], v[66:67], 0, s[72:73]
	s_brev_b32 s0, 32
	v_add_co_u32_e32 v78, vcc, s0, v78
	s_add_i32 s4, s4, s6
	s_nop 0
	v_addc_co_u32_e32 v79, vcc, 0, v79, vcc
	v_lshl_add_u64 v[148:149], v[78:79], 0, s[8:9]
	s_nop 0
	v_lshl_add_u64 v[66:67], v[66:67], 0, s[8:9]
	v_lshl_add_u64 v[68:69], v[68:69], 0, s[8:9]
	v_lshl_add_u64 v[70:71], v[70:71], 0, s[10:11]
	v_lshl_add_u64 v[72:73], v[72:73], 0, s[10:11]
	s_cmpk_lt_i32 s4, 0x4000
	s_waitcnt vmcnt(6)
	v_mov_b64_e32 v[104:105], v[128:129]
	v_mov_b64_e32 v[106:107], v[130:131]
	v_mov_b32_e32 v1, v132
	v_mov_b32_e32 v103, v133
	v_mov_b64_e32 v[56:57], v[134:135]
	v_mov_b64_e32 v[58:59], v[136:137]
	v_mov_b64_e32 v[80:81], v[138:139]
	v_mov_b64_e32 v[78:79], v[140:141]
	s_cbranch_scc0 .Lfin_nopf
	global_load_dwordx4 v[128:131], v[142:143], off
	global_load_dword v132, v[144:145], off offset:128
	global_load_dword v133, v[144:145], off offset:160
	global_load_dwordx4 v[134:137], v[146:147], off
	global_load_dwordx2 v[138:139], v[148:149], off offset:1536
	global_load_dwordx2 v[140:141], v[148:149], off offset:1600
.Lfin_nopf:
	v_cvt_pk_f32_fp8_e32 v[90:91], v106
	v_cvt_pk_f32_fp8_e32 v[82:83], v104
	v_cvt_pk_f32_fp8_sdwa v[92:93], v106 src0_sel:WORD_1
	v_cvt_pk_f32_fp8_sdwa v[84:85], v104 src0_sel:WORD_1
	v_cvt_pk_f32_fp8_e32 v[112:113], v107
	v_cvt_pk_f32_fp8_e32 v[86:87], v105
	v_cvt_pk_f32_fp8_sdwa v[114:115], v107 src0_sel:WORD_1
	v_pk_mul_f32 v[106:107], v[90:91], v[90:91]
	v_pk_mul_f32 v[110:111], v[92:93], v[92:93]
	v_pk_fma_f32 v[106:107], v[82:83], v[82:83], v[106:107]
	v_cvt_pk_f32_fp8_sdwa v[88:89], v105 src0_sel:WORD_1
	v_cvt_pk_f32_fp8_e32 v[104:105], v1
	v_cvt_pk_f32_fp8_sdwa v[116:117], v1 src0_sel:WORD_1
	v_pk_fma_f32 v[110:111], v[84:85], v[84:85], v[110:111]
	v_add_f32_e32 v1, v106, v107
	v_cvt_pk_f32_fp8_e32 v[108:109], v103
	v_pk_mul_f32 v[120:121], v[112:113], v[112:113]
	v_add_f32_e32 v1, v1, v110
	v_pk_fma_f32 v[120:121], v[86:87], v[86:87], v[120:121]
	v_add_f32_e32 v1, v111, v1
	v_cvt_pk_f32_fp8_sdwa v[118:119], v103 src0_sel:WORD_1
	v_pk_mul_f32 v[122:123], v[114:115], v[114:115]
	v_add_f32_e32 v1, v120, v1
	v_pk_fma_f32 v[122:123], v[88:89], v[88:89], v[122:123]
	v_add_f32_e32 v1, v121, v1
	v_pk_mul_f32 v[124:125], v[108:109], v[108:109]
	v_add_f32_e32 v1, v122, v1
	v_pk_fma_f32 v[124:125], v[104:105], v[104:105], v[124:125]
	v_add_f32_e32 v1, v123, v1
	v_pk_mul_f32 v[126:127], v[118:119], v[118:119]
	v_add_f32_e32 v1, v124, v1
	v_pk_fma_f32 v[126:127], v[116:117], v[116:117], v[126:127]
	v_add_f32_e32 v1, v125, v1
	v_add_f32_e32 v1, v126, v1
	v_add_f32_e32 v1, v127, v1
	s_waitcnt lgkmcnt(0)
	s_nop 1
	v_add_f32_dpp v1, v1, v1 quad_perm:[1,0,3,2] row_mask:0xf bank_mask:0xf
	s_waitcnt lgkmcnt(0)
	s_nop 1
	v_add_f32_dpp v1, v1, v1 quad_perm:[2,3,0,1] row_mask:0xf bank_mask:0xf
	s_waitcnt lgkmcnt(0)
	s_nop 1
	v_add_f32_dpp v1, v1, v1 row_half_mirror row_mask:0xf bank_mask:0xf
	v_fmamk_f32 v1, v1, 0x3baaaaab, v220
	v_cmp_gt_f32_e32 vcc, s93, v1
	v_mul_f32_e32 v103, 0x4f800000, v1
	s_nop 0
	v_cndmask_b32_e32 v1, v1, v103, vcc
	v_sqrt_f32_e32 v103, v1
	s_nop 0
	v_add_u32_e32 v106, -1, v103
	v_fma_f32 v107, -v106, v103, v1
	v_cmp_ge_f32_e64 s[0:1], 0, v107
	v_add_u32_e32 v107, 1, v103
	s_nop 0
	v_cndmask_b32_e64 v106, v103, v106, s[0:1]
	v_fma_f32 v103, -v107, v103, v1
	v_cmp_lt_f32_e64 s[0:1], 0, v103
	s_nop 1
	v_cndmask_b32_e64 v103, v106, v107, s[0:1]
	v_mul_f32_e32 v106, 0x37800000, v103
	v_cndmask_b32_e32 v103, v103, v106, vcc
	v_cmp_class_f32_e32 vcc, v1, v221
	s_nop 1
	v_cndmask_b32_e32 v1, v103, v1, vcc
	v_div_scale_f32 v103, s[0:1], v1, v1, s7
	v_rcp_f32_e32 v106, v103
	s_nop 0
	v_fma_f32 v107, -v103, v106, 1.0
	v_fmac_f32_e32 v106, v107, v106
	v_div_scale_f32 v107, vcc, s7, v1, s7
	v_mul_f32_e32 v110, v107, v106
	v_fma_f32 v111, -v103, v110, v107
	v_fmac_f32_e32 v110, v111, v106
	v_fma_f32 v103, -v103, v110, v107
	v_div_fmas_f32 v103, v103, v106, v110
	v_div_fixup_f32 v111, v103, v1, s7
	v_mul_f32_e32 v103, v108, v111
	v_mul_f32_e32 v1, v104, v111
	v_mul_f32_e32 v104, v44, v103
	v_mul_f32_e32 v1, v40, v1
	v_mul_f32_e32 v103, v99, v104
	v_fma_f32 v107, v102, v1, -v103
	v_mul_f32_e32 v103, v99, v1
	v_fmac_f32_e32 v103, v102, v104
	v_mul_f32_e32 v104, v109, v111
	v_mul_f32_e32 v1, v105, v111
	v_mul_f32_e32 v105, v45, v104
	v_mul_f32_e32 v1, v41, v1
	v_mul_f32_e32 v104, v97, v105
	v_fma_f32 v108, v101, v1, -v104
	v_mul_f32_e32 v104, v97, v1
	v_fmac_f32_e32 v104, v101, v105
	v_mul_f32_e32 v105, v118, v111
	v_mul_f32_e32 v1, v116, v111
	v_mul_f32_e32 v106, v46, v105
	v_mul_f32_e32 v1, v42, v1
	v_mul_f32_e32 v105, v96, v106
	v_fma_f32 v109, v100, v1, -v105
	v_mul_f32_e32 v105, v96, v1
	v_fmac_f32_e32 v105, v100, v106
	v_mul_f32_e32 v106, v119, v111
	v_mul_f32_e32 v1, v117, v111
	v_mul_f32_e32 v116, v47, v106
	v_mul_f32_e32 v1, v43, v1
	v_mul_f32_e32 v106, v2, v116
	v_mul_f32_e32 v112, v112, v111
	v_mul_f32_e32 v113, v113, v111
	v_fma_f32 v110, v98, v1, -v106
	v_mul_f32_e32 v106, v2, v1
	v_mul_f32_e32 v1, v114, v111
	v_mul_f32_e32 v114, v115, v111
	v_mul_f32_e32 v112, v20, v112
	v_mul_f32_e32 v113, v21, v113
	v_mov_b32_e32 v115, v3
	v_cvt_pk_fp8_f32 v115, v112, v113
	v_mul_f32_e32 v1, v22, v1
	v_mul_f32_e32 v114, v23, v114
	v_mul_f32_e32 v90, v90, v111
	v_mul_f32_e32 v91, v91, v111
	v_cvt_pk_fp8_f32 v115, v1, v114 op_sel:[0,0,1]
	v_mul_f32_e32 v90, v12, v90
	v_mul_f32_e32 v91, v13, v91
	v_mov_b32_e32 v114, v3
	v_cvt_pk_fp8_f32 v114, v90, v91
	v_mul_f32_e32 v86, v86, v111
	v_mul_f32_e32 v87, v87, v111
	v_mul_f32_e32 v86, v8, v86
	v_mul_f32_e32 v87, v9, v87
	v_mov_b32_e32 v113, v3
	v_mul_f32_e32 v1, v92, v111
	v_mul_f32_e32 v92, v93, v111
	v_cvt_pk_fp8_f32 v113, v86, v87
	v_mul_f32_e32 v82, v82, v111
	v_mul_f32_e32 v83, v83, v111
	v_mul_f32_e32 v1, v14, v1
	v_mul_f32_e32 v92, v15, v92
	v_mul_f32_e32 v82, v4, v82
	v_mul_f32_e32 v83, v5, v83
	v_mov_b32_e32 v112, v3
	v_cvt_pk_fp8_f32 v114, v1, v92 op_sel:[0,0,1]
	v_mul_f32_e32 v1, v88, v111
	v_mul_f32_e32 v88, v89, v111
	v_cvt_pk_fp8_f32 v112, v82, v83
	v_mul_f32_e32 v1, v10, v1
	v_mul_f32_e32 v88, v11, v88
	v_cvt_pk_fp8_f32 v113, v1, v88 op_sel:[0,0,1]
	v_mul_f32_e32 v1, v84, v111
	v_mul_f32_e32 v84, v85, v111
	v_mul_f32_e32 v1, v6, v1
	v_mul_f32_e32 v84, v7, v84
	v_cvt_pk_fp8_f32 v112, v1, v84 op_sel:[0,0,1]
	v_mov_b32_e32 v1, v3
	v_cvt_pk_fp8_f32 v1, v107, v108
	v_add_co_u32_e32 v82, vcc, s14, v76
	v_fmac_f32_e32 v106, v98, v116
	v_cvt_pk_fp8_f32 v1, v109, v110 op_sel:[0,0,1]
	v_addc_co_u32_e32 v83, vcc, 0, v77, vcc
	global_store_dwordx4 v[82:83], v[112:115], off
	v_add_co_u32_e32 v82, vcc, s14, v74
	v_cvt_pk_f32_fp8_e32 v[88:89], v58
	v_addc_co_u32_e32 v83, vcc, 0, v75, vcc
	global_store_dword v[82:83], v1, off offset:128
	v_mov_b32_e32 v1, v3
	v_cvt_pk_fp8_f32 v1, v103, v104
	v_cvt_pk_f32_fp8_sdwa v[90:91], v58 src0_sel:WORD_1
	v_cvt_pk_f32_fp8_sdwa v[84:85], v56 src0_sel:WORD_1
	v_cvt_pk_f32_fp8_e32 v[86:87], v57
	v_cvt_pk_fp8_f32 v1, v105, v106 op_sel:[0,0,1]
	v_cvt_pk_f32_fp8_e32 v[104:105], v59
	v_cvt_pk_f32_fp8_sdwa v[106:107], v59 src0_sel:WORD_1
	v_pk_mul_f32 v[58:59], v[88:89], v[88:89]
	global_store_dword v[82:83], v1, off offset:160
	v_cvt_pk_f32_fp8_e32 v[82:83], v56
	v_pk_mul_f32 v[92:93], v[90:91], v[90:91]
	v_cvt_pk_f32_fp8_sdwa v[56:57], v57 src0_sel:WORD_1
	v_pk_fma_f32 v[92:93], v[84:85], v[84:85], v[92:93]
	v_pk_fma_f32 v[58:59], v[82:83], v[82:83], v[58:59]
	v_pk_mul_f32 v[108:109], v[104:105], v[104:105]
	v_add_f32_e32 v58, v58, v59
	v_add_f32_e32 v58, v58, v92
	v_pk_fma_f32 v[108:109], v[86:87], v[86:87], v[108:109]
	v_add_f32_e32 v58, v93, v58
	v_pk_mul_f32 v[110:111], v[106:107], v[106:107]
	v_add_f32_e32 v58, v108, v58
	v_lshlrev_b32_e32 v1, 16, v80
	v_and_b32_e32 v112, 0xffff0000, v80
	v_lshlrev_b32_e32 v80, 16, v78
	v_pk_fma_f32 v[110:111], v[56:57], v[56:57], v[110:111]
	v_add_f32_e32 v58, v109, v58
	v_add_f32_e32 v58, v110, v58
	v_mul_f32_e32 v59, v80, v80
	v_and_b32_e32 v78, 0xffff0000, v78
	v_add_f32_e32 v58, v111, v58
	v_fmac_f32_e32 v59, v1, v1
	v_add_f32_e32 v58, v59, v58
	v_mul_f32_e32 v59, v78, v78
	v_fmac_f32_e32 v59, v112, v112
	v_and_b32_e32 v110, 0xffff0000, v79
	v_lshlrev_b32_e32 v111, 16, v79
	v_add_f32_e32 v92, v59, v58
	v_and_b32_e32 v108, 0xffff0000, v81
	v_lshlrev_b32_e32 v109, 16, v81
	v_pk_mul_f32 v[58:59], v[110:111], v[110:111]
	s_nop 0
	v_pk_fma_f32 v[58:59], v[108:109], v[108:109], v[58:59]
	s_nop 0
	v_add_f32_e32 v59, v59, v92
	v_add_f32_e32 v58, v58, v59
	s_waitcnt lgkmcnt(0)
	s_nop 1
	v_add_f32_dpp v58, v58, v58 quad_perm:[1,0,3,2] row_mask:0xf bank_mask:0xf
	s_waitcnt lgkmcnt(0)
	s_nop 1
	v_add_f32_dpp v58, v58, v58 quad_perm:[2,3,0,1] row_mask:0xf bank_mask:0xf
	s_waitcnt lgkmcnt(0)
	s_nop 1
	v_add_f32_dpp v58, v58, v58 row_half_mirror row_mask:0xf bank_mask:0xf
	v_fmamk_f32 v58, v58, 0x3baaaaab, v220
	v_cmp_gt_f32_e32 vcc, s93, v58
	v_mul_f32_e32 v59, 0x4f800000, v58
	s_nop 0
	v_cndmask_b32_e32 v58, v58, v59, vcc
	v_sqrt_f32_e32 v59, v58
	s_nop 0
	v_add_u32_e32 v79, -1, v59
	v_fma_f32 v81, -v79, v59, v58
	v_cmp_ge_f32_e64 s[0:1], 0, v81
	v_add_u32_e32 v81, 1, v59
	s_nop 0
	v_cndmask_b32_e64 v79, v59, v79, s[0:1]
	v_fma_f32 v59, -v81, v59, v58
	v_cmp_lt_f32_e64 s[0:1], 0, v59
	s_nop 1
	v_cndmask_b32_e64 v59, v79, v81, s[0:1]
	v_mul_f32_e32 v79, 0x37800000, v59
	v_cndmask_b32_e32 v59, v59, v79, vcc
	v_cmp_class_f32_e32 vcc, v58, v221
	s_nop 1
	v_cndmask_b32_e32 v58, v59, v58, vcc
	v_div_scale_f32 v59, s[0:1], v58, v58, 1.0
	v_rcp_f32_e32 v79, v59
	s_mov_b32 s0, 0x15000000
	v_fma_f32 v81, -v59, v79, 1.0
	v_fmac_f32_e32 v79, v81, v79
	v_div_scale_f32 v81, vcc, 1.0, v58, 1.0
	v_mul_f32_e32 v92, v81, v79
	v_fma_f32 v93, -v59, v92, v81
	v_fmac_f32_e32 v92, v93, v79
	v_fma_f32 v59, -v59, v92, v81
	v_div_fmas_f32 v59, v59, v79, v92
	v_div_fixup_f32 v103, v59, v58, 1.0
	v_mul_f32_e32 v58, v103, v80
	v_mul_f32_e32 v1, v103, v1
	v_mul_f32_e32 v58, v52, v58
	v_mul_f32_e32 v1, v48, v1
	v_mul_f32_e32 v59, v99, v58
	v_fma_f32 v80, v102, v1, -v59
	v_mul_f32_e32 v58, v102, v58
	v_mul_f32_e32 v59, v103, v78
	v_fmac_f32_e32 v58, v99, v1
	v_mul_f32_e32 v1, v103, v112
	v_mul_f32_e32 v59, v53, v59
	v_mul_f32_e32 v1, v49, v1
	v_mul_f32_e32 v78, v97, v59
	v_fma_f32 v81, v101, v1, -v78
	v_mul_f32_e32 v59, v101, v59
	v_mul_f32_e32 v78, v103, v111
	v_fmac_f32_e32 v59, v97, v1
	v_mul_f32_e32 v1, v103, v109
	v_mul_f32_e32 v78, v54, v78
	v_mul_f32_e32 v1, v50, v1
	v_mul_f32_e32 v79, v96, v78
	v_mul_f32_e32 v78, v100, v78
	v_fma_f32 v92, v100, v1, -v79
	v_fmac_f32_e32 v78, v96, v1
	v_mul_f32_e32 v79, v103, v110
	v_mul_f32_e32 v96, v104, v103
	v_mul_f32_e32 v97, v105, v103
	v_mul_f32_e32 v1, v103, v108
	v_mul_f32_e32 v79, v55, v79
	v_mul_f32_e32 v96, v36, v96
	v_mul_f32_e32 v97, v37, v97
	v_mov_b32_e32 v99, v3
	v_mul_f32_e32 v1, v51, v1
	v_mul_f32_e32 v93, v2, v79
	v_cvt_pk_fp8_f32 v99, v96, v97
	v_mul_f32_e32 v88, v88, v103
	v_mul_f32_e32 v89, v89, v103
	v_fma_f32 v93, v98, v1, -v93
	v_mul_f32_e32 v79, v98, v79
	v_mul_f32_e32 v88, v32, v88
	v_mul_f32_e32 v89, v33, v89
	v_mov_b32_e32 v98, v3
	v_fmac_f32_e32 v79, v2, v1
	v_mul_f32_e32 v1, v106, v103
	v_mul_f32_e32 v2, v107, v103
	v_cvt_pk_fp8_f32 v98, v88, v89
	v_mul_f32_e32 v1, v38, v1
	v_mul_f32_e32 v2, v39, v2
	v_cvt_pk_fp8_f32 v99, v1, v2 op_sel:[0,0,1]
	v_mul_f32_e32 v1, v90, v103
	v_mul_f32_e32 v2, v91, v103
	v_mul_f32_e32 v1, v34, v1
	v_mul_f32_e32 v2, v35, v2
	v_cvt_pk_fp8_f32 v98, v1, v2 op_sel:[0,0,1]
	v_mul_f32_e32 v1, v56, v103
	v_mul_f32_e32 v2, v57, v103
	v_mul_f32_e32 v56, v86, v103
	v_mul_f32_e32 v57, v87, v103
	v_mul_f32_e32 v56, v28, v56
	v_mul_f32_e32 v57, v29, v57
	v_mov_b32_e32 v97, v3
	v_cvt_pk_fp8_f32 v97, v56, v57
	v_mul_f32_e32 v56, v82, v103
	v_mul_f32_e32 v57, v83, v103
	v_mul_f32_e32 v56, v24, v56
	v_mul_f32_e32 v57, v25, v57
	v_mov_b32_e32 v96, v3
	v_cvt_pk_fp8_f32 v96, v56, v57
	v_mul_f32_e32 v1, v30, v1
	v_mul_f32_e32 v2, v31, v2
	v_cvt_pk_fp8_f32 v97, v1, v2 op_sel:[0,0,1]
	v_mul_f32_e32 v1, v84, v103
	v_mul_f32_e32 v2, v85, v103
	v_mul_f32_e32 v1, v26, v1
	v_mul_f32_e32 v2, v27, v2
	v_cvt_pk_fp8_f32 v96, v1, v2 op_sel:[0,0,1]
	v_mov_b32_e32 v1, v3
	v_cvt_pk_fp8_f32 v1, v80, v81
	v_add_co_u32_e32 v56, vcc, s0, v76
	v_cvt_pk_fp8_f32 v1, v92, v93 op_sel:[0,0,1]
	s_nop 0
	v_addc_co_u32_e32 v57, vcc, 0, v77, vcc
	global_store_dwordx4 v[56:57], v[96:99], off
	v_add_co_u32_e32 v56, vcc, 0x15000000, v74
	s_nop 1
	v_addc_co_u32_e32 v57, vcc, 0, v75, vcc
	global_store_dword v[56:57], v1, off offset:128
	v_mov_b32_e32 v1, v3
	v_cvt_pk_fp8_f32 v1, v58, v59
	v_cvt_pk_fp8_f32 v1, v78, v79 op_sel:[0,0,1]
	global_store_dword v[56:57], v1, off offset:160
	s_cbranch_scc1 .LBB0_596
